# NA unit prologue: bias-table wait/convert/LDS write deferred behind the Q loads and first LDS-DMA pieces (one round trip instead of two)
# speedup vs baseline: 1.0155x; 1.0014x over previous
; DEV unsigned lds_addr(LAS char* p) { return (unsigned)(uintptr_t)p; }
; #define NA_ISSUE(j_, st_) do { const int ti_ = (j_) < ntl ? T0 + (j_) : 256 + (j_) - ntl; const unsigned char* s_ = imgs + (size_t)ti_ * 16384 + wid * 2048 + lane * 16; const unsigned d_ = ldsw + (unsigned)((st_) * STG); \
;     glds16a(s_, d_); glds16a(s_ + 1024, d_ + 1024); } while (0)
; DEV void na_unit(const Params& p, int layer, int b, int hd, int rg, bool ctxq, LAS char* lds) {
;     ...
;         for (int i = tid; i < 15 * 128; i += 512) { const int dr = i >> 7, d = (i & 127) - 64; tb[i] = (d >= -15 && d <= 15) ? p.b_rpb[((layer * 6 + hd) * 15 + dr) * 31 + d + 15] * LOG2E : -1e30f; }
;     } else tok = NLAT + b * 256 + 32 * wid + r;
;     const int nt = ntl + 4;
;     bf16x8 qf[4];
; #pragma unroll
;     for (int d0 = 0; d0 < 4; ++d0) qf[d0] = *(const bf16x8*)((const bf16_t*)(ws + WS_QB) + (size_t)tok * 384 + hd * 64 + 16 * d0 + 8 * h);
;     const unsigned char* imgs = ws + WS_KVB + (size_t)((b * 6 + hd) * 260) * 16384;
;     const unsigned ldsw = (unsigned)__builtin_amdgcn_readfirstlane((int)(lds_addr(lds) + (unsigned)(wid * 2048)));
;     ...
;     NA_ISSUE(0, 0); NA_ISSUE(1, 1);
.LBB0_666:
	v_mov_b32_e32 v162, 0xf149f2ca
	v_mov_b32_e32 v163, 0xf149f2ca
	v_mov_b32_e32 v164, 0xf149f2ca
	v_mov_b32_e32 v165, 0xf149f2ca
	s_movk_i32 s2, 0x180
	v_cmp_gt_u32_e64 s[20:21], s2, v4
	s_and_saveexec_b64 s[40:41], vcc
	s_cbranch_execz .Lna_tb_fill
	v_ashrrev_i32_e32 v6, 7, v4
	v_add_u32_e32 v6, s19, v6
	v_mul_lo_u32 v6, v6, 31
	v_ashrrev_i32_e32 v7, 31, v6
	v_lshl_add_u64 v[6:7], v[178:179], 0, v[6:7]
	v_lshl_add_u64 v[6:7], v[6:7], 2, s[72:73]
	global_load_dword v162, v[6:7], off offset:-196
	global_load_dword v163, v[6:7], off offset:300
	global_load_dword v164, v[6:7], off offset:796
	s_and_b64 exec, exec, s[20:21]
	global_load_dword v165, v[6:7], off offset:1292
.Lna_tb_fill:
	s_or_b64 exec, exec, s[40:41]
.LBB0_668:
	s_or_b64 exec, exec, s[8:9]
	s_lshl_b32 s2, s13, 2
	v_ashrrev_i32_e32 v19, 7, v18
	v_ashrrev_i32_e32 v2, 6, v18
	s_and_b32 s2, s2, 0xfc
	v_and_b32_e32 v4, -2, v19
	v_add_u32_e32 v7, s2, v4
	v_bfe_u32 v20, v18, 4, 1
	v_lshlrev_b32_e32 v4, 4, v2
	v_or_b32_e32 v9, v7, v20
	v_and_b32_e32 v8, 48, v4
	v_and_b32_e32 v21, 15, v18
	s_lshl_b32 s3, s18, 14
	v_or_b32_e32 v6, v8, v21
	v_lshl_add_u32 v4, v9, 6, s3
	v_or_b32_e32 v98, v4, v6
	v_mov_b64_e32 v[4:5], s[6:7]
	s_movk_i32 s3, 0x300
	v_mad_i64_i32 v[4:5], s[8:9], v98, s3, v[4:5]
	s_lshl_b32 s8, s17, 6
	v_bfe_u32 v22, v18, 5, 1
	s_ashr_i32 s9, s8, 31
	v_lshl_add_u64 v[4:5], s[8:9], 1, v[4:5]
	v_lshlrev_b32_e32 v100, 4, v22
	v_mov_b32_e32 v101, v179
	v_lshl_add_u64 v[4:5], v[4:5], 0, v[100:101]
	s_mov_b64 s[18:19], 0x2e640100
	s_mov_b32 s3, 0x2e640000
	v_lshl_add_u64 v[10:11], v[4:5], 0, s[18:19]
	v_add_co_u32_e32 v4, vcc, s3, v4
	s_max_u32 s3, s2, 4
	s_nop 0
	v_addc_co_u32_e32 v5, vcc, 0, v5, vcc
	global_load_dwordx4 v[82:85], v[10:11], off offset:32
	global_load_dwordx4 v[86:89], v[10:11], off offset:64
	global_load_dwordx4 v[90:93], v[4:5], off offset:256
	global_load_dwordx4 v[94:97], v[10:11], off offset:96
	v_sub_u32_e64 v4, s2, 1 clamp
	v_sub_u32_e64 v5, s2, 4 clamp
	v_readfirstlane_b32 s2, v4
	s_mulk_i32 s16, 0x104
	s_min_u32 s2, s2, 0xf8
	s_ashr_i32 s17, s16, 31
	s_sub_i32 s18, s2, s3
	s_lshl_b64 s[16:17], s[16:17], 14
	s_add_u32 s2, s6, s16
	s_addc_u32 s16, s7, s17
	s_add_u32 s20, s2, 0x2fea0100
	v_lshlrev_b32_e32 v4, 11, v2
	s_addc_u32 s21, s16, 0
	v_readfirstlane_b32 s16, v4
	s_add_i32 s16, s16, 0
	s_sub_i32 s2, 0xf4, s18
	s_cmp_gt_i32 s18, -12
	v_mov_b32_e32 v2, s2
	s_cselect_b64 vcc, -1, 0
	v_cndmask_b32_e32 v178, v2, v5, vcc
	v_lshlrev_b64 v[10:11], 14, v[178:179]
	v_and_b32_e32 v23, 63, v18
	v_lshl_add_u64 v[10:11], s[20:21], 0, v[10:11]
	v_ashrrev_i32_e32 v5, 31, v4
	v_lshl_add_u64 v[10:11], v[10:11], 0, v[4:5]
	v_lshlrev_b32_e32 v178, 4, v23
	v_lshl_add_u64 v[10:11], v[10:11], 0, v[178:179]
	s_mov_b32 s2, m0
	s_mov_b32 m0, s16
	s_nop 0
	global_load_lds_dwordx4 v[10:11], off
	s_mov_b32 m0, s2
	s_add_i32 s2, s16, 0x400
	v_lshl_add_u64 v[10:11], v[10:11], 0, s[10:11]
	s_mov_b32 s17, m0
	s_mov_b32 m0, s2
	s_nop 0
	global_load_lds_dwordx4 v[10:11], off
	s_mov_b32 m0, s17
	s_add_i32 s3, s3, -3
	s_sub_i32 s2, 0xf5, s18
	s_cmp_gt_i32 s18, -11
	s_cselect_b32 s30, s3, s2
	s_lshl_b64 s[36:37], s[30:31], 14
	s_add_u32 s36, s20, s36
	s_addc_u32 s37, s21, s37
	v_lshl_add_u64 v[10:11], s[36:37], 0, v[4:5]
	v_lshl_add_u64 v[10:11], v[10:11], 0, v[178:179]
	s_add_i32 s2, s16, 0x4000
	s_mov_b32 s3, m0
	s_mov_b32 m0, s2
	s_nop 0
	global_load_lds_dwordx4 v[10:11], off
	s_mov_b32 m0, s3
	v_lshl_add_u64 v[10:11], v[10:11], 0, s[10:11]
	s_add_i32 s2, s16, 0x4400
	s_mov_b32 s3, m0
	s_mov_b32 m0, s2
	s_nop 0
	global_load_lds_dwordx4 v[10:11], off
	s_mov_b32 m0, s3
	s_cmp_gt_i32 s18, -16
	s_mov_b64 s[40:41], -1
	s_cbranch_scc1 .LBB0_670
	v_lshlrev_b32_e32 v2, 4, v22
	s_mov_b64 s[40:41], 0
; DEV unsigned lds_addr(LAS char* p) { return (unsigned)(uintptr_t)p; }
; #define NA_ISSUE(j_, st_) do { const int ti_ = (j_) < ntl ? T0 + (j_) : 256 + (j_) - ntl; const unsigned char* s_ = imgs + (size_t)ti_ * 16384 + wid * 2048 + lane * 16; const unsigned d_ = ldsw + (unsigned)((st_) * STG); \
;     glds16a(s_, d_); glds16a(s_ + 1024, d_ + 1024); } while (0)
; DEV void na_unit(const Params& p, int layer, int b, int hd, int rg, bool ctxq, LAS char* lds) {
;     ...
;         for (int i = tid; i < 15 * 128; i += 512) { const int dr = i >> 7, d = (i & 127) - 64; tb[i] = (d >= -15 && d <= 15) ? p.b_rpb[((layer * 6 + hd) * 15 + dr) * 31 + d + 15] * LOG2E : -1e30f; }
;     } else tok = NLAT + b * 256 + 32 * wid + r;
;     const int nt = ntl + 4;
;     bf16x8 qf[4];
; #pragma unroll
;     for (int d0 = 0; d0 < 4; ++d0) qf[d0] = *(const bf16x8*)((const bf16_t*)(ws + WS_QB) + (size_t)tok * 384 + hd * 64 + 16 * d0 + 8 * h);
;     const unsigned char* imgs = ws + WS_KVB + (size_t)((b * 6 + hd) * 260) * 16384;
;     const unsigned ldsw = (unsigned)__builtin_amdgcn_readfirstlane((int)(lds_addr(lds) + (unsigned)(wid * 2048)));
;     ...
;     NA_ISSUE(0, 0); NA_ISSUE(1, 1);
;     f32x16 o[2];
; #pragma unroll
;     for (int dh = 0; dh < 2; ++dh)
; #pragma unroll
;         for (int i = 0; i < 16; ++i) o[dh][i] = 0.f;
;     float lsum = 0.f;
;     const int c0 = min(max(cq - 8, 0), 48);
;     int st = 0, stn = 2;
.LBB0_670:
	v_mov_b32_e32 v65, 0
	s_andn2_b64 vcc, exec, s[40:41]
	v_mov_b32_e32 v64, v65
	v_mov_b32_e32 v63, v65
	v_mov_b32_e32 v62, v65
	v_mov_b32_e32 v61, v65
	v_mov_b32_e32 v60, v65
	v_mov_b32_e32 v59, v65
	v_mov_b32_e32 v58, v65
	v_mov_b32_e32 v57, v65
	v_mov_b32_e32 v56, v65
	v_mov_b32_e32 v55, v65
	v_mov_b32_e32 v54, v65
	v_mov_b32_e32 v53, v65
	v_mov_b32_e32 v52, v65
	v_mov_b32_e32 v51, v65
	v_mov_b32_e32 v50, v65
	v_mov_b32_e32 v81, v65
	v_mov_b32_e32 v80, v65
	v_mov_b32_e32 v79, v65
	v_mov_b32_e32 v78, v65
	v_mov_b32_e32 v77, v65
	v_mov_b32_e32 v76, v65
	v_mov_b32_e32 v75, v65
	v_mov_b32_e32 v74, v65
	v_mov_b32_e32 v73, v65
	v_mov_b32_e32 v72, v65
	v_mov_b32_e32 v71, v65
	v_mov_b32_e32 v70, v65
	v_mov_b32_e32 v69, v65
	v_mov_b32_e32 v68, v65
	v_mov_b32_e32 v67, v65
	v_mov_b32_e32 v66, v65
	v_mov_b32_e32 v118, v65
	s_waitcnt vmcnt(8)
	v_mul_f32_e32 v162, 0x3fb8aa3b, v162
	v_mul_f32_e32 v163, 0x3fb8aa3b, v163
	v_mul_f32_e32 v164, 0x3fb8aa3b, v164
	v_mul_f32_e32 v165, 0x3fb8aa3b, v165
	v_lshlrev_b32_e32 v166, 2, v246
	v_add_u32_e32 v166, 0xc000, v166
	ds_write_b32 v166, v162
	ds_write_b32 v166, v163 offset:2048
	ds_write_b32 v166, v164 offset:4096
	ds_write_b32 v166, v165 offset:6144
	s_cbranch_vccnz .LBB0_652
	v_max_i32_e32 v2, 4, v9
	v_add_u32_e32 v2, -4, v2
	v_min_u32_e32 v99, 0xf8, v2
	v_max_i32_e32 v2, 4, v7
	v_add_u32_e32 v2, -4, v2
	v_min_u32_e32 v101, 0xf8, v2
	v_max_i32_e32 v2, 3, v7
	v_add_u32_e32 v2, -3, v2
	v_min_u32_e32 v2, 0xf8, v2
	s_bfe_u32 s2, s12, 0x60002
	v_add_u32_e32 v104, 8, v2
	v_sub_u32_e64 v2, v8, 8 clamp
	s_lshl_b32 s3, s2, 2
	v_min_u32_e32 v25, 32, v2
	v_sub_u32_e64 v2, s3, 1 clamp
	v_lshlrev_b32_e32 v27, 1, v23
	v_lshlrev_b32_e32 v23, 3, v23
	s_max_u32 s28, s3, 4
	v_readfirstlane_b32 s3, v2
	v_max_i32_e32 v2, 8, v6
	v_and_b32_e32 v107, 32, v27
	v_and_b32_e32 v108, 24, v23
	v_lshrrev_b32_e32 v23, 3, v18
	v_bfe_u32 v27, v18, 2, 2
	v_add_u32_e32 v2, -8, v2
	v_lshlrev_b32_e32 v105, 10, v22
	v_and_or_b32 v23, v23, 4, v27
	v_lshlrev_b32_e32 v22, 2, v22
	v_min_u32_e32 v26, 48, v2
	v_lshlrev_b32_e32 v109, 6, v23
	v_or_b32_e32 v23, v25, v22
	v_or_b32_e32 v22, v22, v27
	v_lshlrev_b32_e32 v114, 6, v22
	v_sub_u32_e32 v22, v23, v26
	v_add_u32_e32 v23, -15, v22
	v_cmp_gt_u32_e64 s[42:43], -16, v23
	v_add_u32_e32 v23, -14, v22
	v_cmp_gt_u32_e64 s[44:45], -16, v23
	v_add_u32_e32 v23, -13, v22
	v_cmp_gt_u32_e64 s[46:47], -16, v23
	v_add_u32_e32 v23, -8, v22
	v_cmp_gt_u32_e64 s[48:49], -16, v23
	v_add_u32_e32 v23, -7, v22
	v_cmp_gt_u32_e64 s[50:51], -16, v23
	v_add_u32_e32 v23, -6, v22
	v_cmp_gt_u32_e64 s[52:53], -16, v23
	v_add_u32_e32 v23, -5, v22
	v_cmp_gt_u32_e64 s[54:55], -16, v23
	v_add_u32_e32 v23, 1, v22
	v_cmp_gt_u32_e64 s[58:59], -16, v23
	v_add_u32_e32 v23, 2, v22
	v_cmp_gt_u32_e64 s[60:61], -16, v23
	v_add_u32_e32 v23, 3, v22
	v_cmp_gt_u32_e64 s[62:63], -16, v23
	v_add_u32_e32 v23, 8, v22
	v_cmp_gt_u32_e64 s[64:65], -16, v23
	v_add_u32_e32 v23, 9, v22
	v_cmp_lt_u32_e64 s[40:41], 15, v22
	v_cmp_gt_u32_e64 s[56:57], -16, v22
	v_cmp_gt_u32_e64 s[66:67], -16, v23
	v_add_u32_e32 v23, 10, v22
	v_add_u32_e32 v22, 11, v22
	v_and_b32_e32 v24, 31, v18
	v_cmp_gt_u32_e64 s[70:71], -16, v22
	v_lshl_or_b32 v22, s28, 9, v100
	v_lshlrev_b32_e32 v106, 4, v24
	v_add_lshl_u32 v110, v25, v24, 4
	v_lshlrev_b32_e32 v24, 1, v18
	v_lshl_add_u32 v22, v25, 2, v22
	v_lshlrev_b32_e32 v21, 2, v21
	v_and_b32_e32 v112, 32, v24
	v_lshlrev_b32_e32 v24, 3, v18
	v_sub_u32_e32 v21, v22, v21
	v_and_b32_e32 v18, 0xc0, v18
	v_sub_u32_e32 v18, v21, v18
	v_lshlrev_b32_e32 v20, 9, v20
	v_lshlrev_b32_e32 v19, 9, v19
	v_sub_u32_e32 v18, v18, v20
	v_and_b32_e32 v19, 0xfffffc00, v19
	s_lshl_b32 s2, s2, 11
	v_sub_u32_e32 v18, v18, v19
	v_lshl_add_u64 v[4:5], s[20:21], 0, v[4:5]
	s_min_u32 s3, s3, 0xf8
	s_waitcnt vmcnt(0)
	v_xor_b32_e32 v2, 0x80000000, v3
	v_subrev_u32_e32 v18, s2, v18
	v_readlane_b32 s2, v253, 56
	v_mov_b32_e32 v117, 0
	s_add_i32 s17, s18, 16
	v_lshl_add_u64 v[102:103], v[4:5], 0, v[178:179]
	s_add_i32 s18, s18, 12
	s_mov_b32 s19, 2
	s_sub_i32 s30, s28, s3
	v_mov_b32_e32 v3, v2
	v_mov_b32_e32 v4, v2
	v_mov_b32_e32 v5, v2
	v_mov_b32_e32 v6, v2
	v_mov_b32_e32 v7, v2
	v_mov_b32_e32 v8, v2
	v_mov_b32_e32 v9, v2
	v_mov_b32_e32 v10, v2
	v_mov_b32_e32 v11, v2
	v_mov_b32_e32 v12, v2
	v_mov_b32_e32 v13, v2
	v_mov_b32_e32 v14, v2
	v_mov_b32_e32 v15, v2
	v_mov_b32_e32 v16, v2
	v_mov_b32_e32 v17, v2
	v_lshlrev_b32_e32 v111, 6, v25
	v_and_b32_e32 v113, 24, v24
	v_add_u32_e32 v115, 8, v99
	v_cmp_gt_u32_e64 s[68:69], -16, v23
	v_add_u32_e32 v116, s2, v18
	s_mov_b32 s75, 0
	s_mov_b32 s33, 0
	v_mov_b32_e32 v18, 0
	v_mov_b32_e32 v19, v117
	v_mov_b32_e32 v20, v117
	v_mov_b32_e32 v21, v117
	v_mov_b32_e32 v22, v117
	v_mov_b32_e32 v23, v117
	v_mov_b32_e32 v24, v117
	v_mov_b32_e32 v25, v117
	v_mov_b32_e32 v26, v117
	v_mov_b32_e32 v27, v117
	v_mov_b32_e32 v28, v117
	v_mov_b32_e32 v29, v117
	v_mov_b32_e32 v30, v117
	v_mov_b32_e32 v31, v117
	v_mov_b32_e32 v32, v117
	v_mov_b32_e32 v33, v117
	v_mov_b32_e32 v34, 0
	v_mov_b32_e32 v35, v117
	v_mov_b32_e32 v36, v117
	v_mov_b32_e32 v37, v117
	v_mov_b32_e32 v38, v117
	v_mov_b32_e32 v39, v117
	v_mov_b32_e32 v40, v117
	v_mov_b32_e32 v41, v117
	v_mov_b32_e32 v42, v117
	v_mov_b32_e32 v43, v117
	v_mov_b32_e32 v44, v117
	v_mov_b32_e32 v45, v117
	v_mov_b32_e32 v46, v117
	v_mov_b32_e32 v47, v117
	v_mov_b32_e32 v48, v117
	v_mov_b32_e32 v49, v117
	s_add_i32 s36, s75, 1
	s_cmp_ge_i32 s36, s17
	s_mov_b64 s[20:21], -1
	s_cbranch_scc0 .LBB0_674
	s_branch .LBB0_673
